# out-proj GEMM unit order: 16 row tiles x 2 col tiles per XCD round with the column pair rotated by XCD parity (weight panels shared by 16 workgroups, XCD halves decorrelated)
# baseline (speedup 1.0000x reference)
.LBB0_210:
	s_or_b64 exec, exec, s[0:1]
	s_waitcnt lgkmcnt(0)
	s_barrier
	s_load_dword s5, s[94:95], 0x180
	s_mov_b64 s[0:1], src_shared_base
	v_writelane_b32 v252, s0, 6
	s_mov_b32 s51, 0
	s_movk_i32 s93, 0x180
	v_writelane_b32 v252, s1, 7
	s_waitcnt lgkmcnt(0)
	s_ashr_i32 s7, s5, 3
	v_readlane_b32 s4, v252, 0
	s_ashr_i32 s6, s4, 3
	s_cmpk_lt_i32 s6, 0x120
	s_cselect_b64 s[0:1], -1, 0
	v_writelane_b32 v252, s0, 8
	s_movk_i32 s77, 0x70
	s_mov_b32 s85, 0x800000
	v_writelane_b32 v252, s1, 9
	s_lshl_b32 s0, s4, 4
	s_and_b32 s8, s0, 0x70
	s_lshr_b32 s100, s6, 5
	s_and_b32 s101, s6, 31
	s_lshr_b32 s0, s100, 2
	s_lshl_b32 s0, s0, 3
	s_and_b32 s1, s101, 7
	s_add_i32 s0, s0, s1
	s_lshr_b32 s11, s8, 4
	s_add_i32 s10, s100, s11
	s_and_b32 s10, s10, 3
	s_lshl_b32 s10, s10, 2
	s_lshr_b32 s1, s101, 3
	s_add_i32 s10, s10, s1
	s_and_b32 s1, s101, 15
	s_lshr_b32 s11, s101, 4
	s_add_i32 s11, s11, 16
	s_cmp_lt_u32 s100, 8
	s_cselect_b32 s0, s0, s1
	s_cselect_b32 s10, s10, s11
	s_add_i32 s2, s0, s8
	s_ashr_i32 s11, s10, 31
	s_lshl_b64 s[0:1], s[10:11], 19
	v_writelane_b32 v252, s0, 10
	s_waitcnt vmcnt(0)
	v_mov_b32_e32 v3, 0
	v_mov_b32_e32 v220, 0x1000
	v_writelane_b32 v252, s1, 11
	s_mov_b32 s0, s10
	v_writelane_b32 v252, s0, 12
	v_mov_b32_e32 v221, 0x2000
	v_mov_b32_e32 v219, 0x3b808081
	v_writelane_b32 v252, s1, 13
	s_add_i32 s0, s10, -12
	s_cmp_lt_u32 s0, 3
	s_cselect_b64 s[0:1], -1, 0
	v_writelane_b32 v252, s0, 14
	s_ashr_i32 s3, s2, 31
	v_mbcnt_hi_u32_b32 v214, -1, v42
	v_writelane_b32 v252, s1, 15
	s_lshl_b64 s[0:1], s[2:3], 19
	v_writelane_b32 v252, s0, 16
	v_mov_b32_e32 v226, 0x180
	v_mov_b32_e32 v232, 0x100000
	v_writelane_b32 v252, s1, 17
	s_mov_b32 s0, s2
	v_writelane_b32 v252, s0, 18
	v_mov_b32_e32 v227, 0x2080
	v_mov_b32_e32 v228, 0xff61b1e6
	v_writelane_b32 v252, s1, 19
	s_lshl_b32 s0, s2, 8
	s_cmpk_eq_i32 s5, 0x100
	v_writelane_b32 v252, s0, 20
	s_cselect_b64 s[0:1], -1, 0
	s_ashr_i32 s10, s4, 4
	v_writelane_b32 v252, s0, 21
	s_ashr_i32 s11, s10, 31
	s_and_b32 s9, s4, 15
	v_writelane_b32 v252, s1, 22
	s_lshl_b64 s[0:1], s[10:11], 2
	s_getpc_b64 s[2:3]
	s_add_u32 s2, s2, __const._Z4mega6Params.SLOT@rel32@lo+4
	s_addc_u32 s3, s3, __const._Z4mega6Params.SLOT@rel32@hi+12
	s_add_u32 s0, s2, s0
	s_addc_u32 s1, s3, s1
	v_writelane_b32 v252, s0, 23
	s_mov_b32 s2, s10
	v_mov_b32_e32 v233, 0xc8
	v_writelane_b32 v252, s1, 24
	s_lshl_b32 s0, s9, 5
	v_writelane_b32 v252, s0, 25
	s_add_i32 s0, s4, 0xffffff70
	v_writelane_b32 v252, s2, 26
	s_add_i32 s1, s10, -9
	s_cmp_lt_u32 s1, 4
	s_cselect_b32 s0, s0, 0x100000
	v_writelane_b32 v252, s3, 27
	v_writelane_b32 v252, s0, 28
	s_lshl_b32 s0, s9, 3
	s_add_i32 s1, s0, -1
	s_lshl_b32 s0, s9, 2
	v_writelane_b32 v252, s9, 29
	s_sub_i32 s0, s1, s0
	v_writelane_b32 v252, s1, 30
	s_cmpk_lt_i32 s6, 0x100
	v_writelane_b32 v252, s0, 31
	s_cselect_b64 s[0:1], -1, 0
	v_writelane_b32 v252, s0, 32
	v_mov_b32_e32 v234, 0xc0
	s_movk_i32 s91, 0xc0
	v_writelane_b32 v252, s1, 33
	s_lshr_b32 s100, s6, 5
	s_and_b32 s101, s6, 31
	s_lshr_b32 s1, s100, 2
	s_lshl_b32 s1, s1, 3
	s_and_b32 s0, s101, 7
	s_add_i32 s1, s1, s0
	s_lshr_b32 s0, s8, 4
	s_add_i32 s2, s100, s0
	s_and_b32 s2, s2, 3
	s_lshl_b32 s2, s2, 2
	s_lshr_b32 s0, s101, 3
	s_add_i32 s2, s2, s0
	v_writelane_b32 v252, s8, 34
	s_add_i32 s8, s1, s8
	s_add_i32 s3, s2, 18
	s_cmp_lt_i32 s2, 0
	s_cselect_b64 s[0:1], -1, 0
	v_writelane_b32 v252, s0, 35
	s_movk_i32 s33, 0x2400
	s_movk_i32 s96, 0xc00
	v_writelane_b32 v252, s1, 36
	s_and_b64 s[0:1], s[0:1], exec
	s_cselect_b32 s50, s3, s2
	v_writelane_b32 v252, s3, 37
	s_lshl_b64 s[0:1], s[50:51], 19
	s_add_i32 s2, s2, 6
	v_writelane_b32 v252, s0, 38
	s_cmp_lt_u32 s2, 3
	s_movk_i32 s97, 0x60
	v_writelane_b32 v252, s1, 39
	s_cselect_b64 s[0:1], -1, 0
	v_writelane_b32 v252, s0, 40
	s_ashr_i32 s9, s8, 31
	s_mov_b32 s83, 0x2aaaaaab
	v_writelane_b32 v252, s1, 41
	s_lshl_b64 s[0:1], s[8:9], 19
	v_writelane_b32 v252, s0, 42
	s_movk_i32 s86, 0xff40
	s_movk_i32 s87, 0x7fff
	v_writelane_b32 v252, s1, 43
	s_mov_b32 s0, s8
	v_writelane_b32 v252, s0, 44
	s_movk_i32 s88, 0x9ff
	s_movk_i32 s89, 0x2080
	v_writelane_b32 v252, s1, 45
	s_lshl_b32 s0, s8, 8
	s_cmpk_lt_i32 s6, 0x80
	v_writelane_b32 v252, s0, 46
	s_cselect_b64 s[0:1], -1, 0
	v_writelane_b32 v252, s0, 47
	s_mov_b32 s90, 0xff61b1e6
	s_mov_b64 s[60:61], 0x80
	v_writelane_b32 v252, s1, 48
	s_and_b32 s0, s4, 7
	s_cmp_lt_i32 s6, 64
	s_cselect_b64 s[2:3], -1, 0
	v_writelane_b32 v252, s2, 49
	s_mov_b64 s[40:41], 0x2200
	s_mov_b64 s[70:71], 0x2000
	v_writelane_b32 v252, s3, 50
	v_writelane_b32 v252, s0, 51
	s_lshl_b32 s2, s0, 4
	s_lshr_b32 s100, s6, 5
	s_add_i32 s100, s100, s0
	s_and_b32 s100, s100, 1
	s_lshl_b32 s100, s100, 1
	s_and_b32 s101, s6, 31
	s_and_b32 s1, s101, 15
	v_writelane_b32 v252, s2, 52
	s_add_i32 s1, s2, s1
	s_lshr_b32 s101, s101, 4
	v_writelane_b32 v252, s1, 53
	s_add_i32 s8, s100, s101
	s_lshl_b32 s0, s5, 3
	v_writelane_b32 v252, s0, 54
	s_mov_b64 s[80:81], 0x48000
	s_mov_b32 s82, 0x3e38aa3b
	v_writelane_b32 v252, s1, 55
	s_lshl_b32 s0, s5, 5
	v_writelane_b32 v252, s0, 56
	s_ashr_i32 s0, s4, 6
	v_writelane_b32 v252, s0, 57
	s_and_b32 s0, s6, 7
	s_cmp_lt_u32 s0, 4
	v_writelane_b32 v252, s0, 58
	s_cselect_b64 s[0:1], -1, 0
	s_abs_i32 s2, s7
	v_cvt_f32_u32_e32 v1, s2
	v_writelane_b32 v252, s0, 59
	s_mov_b32 s5, s51
	s_ashr_i32 s9, s8, 31
	v_rcp_iflag_f32_e32 v1, v1
	v_writelane_b32 v252, s1, 60
	v_writelane_b32 v252, s7, 61
	s_and_b32 s1, s6, 1
	v_mul_f32_e32 v1, 0x4f7ffffe, v1
	v_cvt_u32_f32_e32 v1, v1
	v_writelane_b32 v252, s6, 62
	s_lshl_b32 s4, s1, 7
	v_writelane_b32 v252, s4, 63
	s_lshl_b32 s1, s1, 1
	s_lshl_b32 s0, s6, 18
	v_writelane_b32 v253, s5, 0
	v_writelane_b32 v253, s1, 1
	v_writelane_b32 v253, s2, 2
	s_sub_i32 s1, 0, s2
	v_readfirstlane_b32 s2, v1
	s_mul_i32 s1, s1, s2
	s_mul_hi_u32 s1, s2, s1
	s_add_i32 s1, s2, s1
	v_writelane_b32 v253, s1, 3
	s_add_i32 s1, 0, 0x26280
	v_writelane_b32 v253, s1, 4
	s_add_i32 s1, 0, 0x26284
	v_writelane_b32 v253, s1, 5
	s_add_i32 s1, 0, 0x26288
	v_writelane_b32 v253, s1, 6
	s_add_i32 s1, 0, 0x18400
	v_writelane_b32 v253, s1, 7
	s_add_i32 s1, 0, 0x184c0
	v_writelane_b32 v253, s1, 8
	s_add_i32 s1, 0, 0x17700
	v_writelane_b32 v253, s1, 9
	s_add_i32 s1, 0, 0x17800
	v_writelane_b32 v253, s1, 10
	s_add_i32 s1, 0, 0x17100
	v_writelane_b32 v253, s1, 11
	s_add_i32 s1, 0, 0xb600
	v_writelane_b32 v253, s1, 12
	s_add_i32 s1, 0, 0x1e650
	v_writelane_b32 v253, s1, 13
	s_add_i32 s1, 0, 0x5c00
	v_writelane_b32 v253, s1, 14
	s_add_i32 s1, 0, 0x15940
	v_writelane_b32 v253, s1, 15
	s_add_i32 s1, 0, 0x15840
	v_writelane_b32 v253, s1, 16
	s_add_i32 s1, 0, 0x15f40
	v_writelane_b32 v253, s1, 17
	s_add_i32 s1, 0, 0x15240
	v_writelane_b32 v253, s1, 18
	s_add_i32 s1, 0, 0x11640
	v_writelane_b32 v253, s1, 19
	s_add_i32 s1, 0, 0x14640
	v_writelane_b32 v253, s1, 20
	s_add_i32 s1, 0, 0x14c40
	v_writelane_b32 v253, s1, 21
	s_add_i32 s1, 0, 0x15c40
	v_writelane_b32 v253, s1, 22
	s_add_i32 s1, 0, 0x15d00
	v_writelane_b32 v253, s1, 23
	s_add_i32 s1, 0, 0x15dc0
	v_writelane_b32 v253, s1, 24
	s_add_i32 s1, 0, 0x15e80
	v_writelane_b32 v253, s1, 25
	s_add_i32 s1, 0, 0x7e40
	v_writelane_b32 v253, s1, 26
	s_add_i32 s1, 0, 0x8280
	v_writelane_b32 v253, s1, 27
	s_add_i32 s1, 0, 0xa094
	v_writelane_b32 v253, s1, 28
	s_add_i32 s1, 0, 0x10380
	v_writelane_b32 v253, s1, 29
	s_add_i32 s1, 0, 0x12380
	v_writelane_b32 v253, s1, 30
	s_add_i32 s1, 0, 0x14380
	v_writelane_b32 v253, s1, 31
	s_add_i32 s1, 0, 0x16380
	v_writelane_b32 v253, s1, 32
	s_add_i32 s1, 0, 0x18380
	v_writelane_b32 v253, s1, 33
	s_add_i32 s1, 0, 0x1a380
	v_writelane_b32 v253, s1, 34
	s_add_i32 s1, 0, 0x1c380
	v_writelane_b32 v253, s1, 35
	s_add_i32 s1, 0, 0x1e380
	v_writelane_b32 v253, s1, 36
	s_add_i32 s1, 0, 0x10100
	v_writelane_b32 v253, s1, 37
	s_add_i32 s1, 0, 0x12100
	v_writelane_b32 v253, s1, 38
	s_add_i32 s1, 0, 0x16100
	v_writelane_b32 v253, s1, 39
	s_add_i32 s1, 0, 0x20060
	v_writelane_b32 v253, s1, 40
	s_add_i32 s1, 0, 0x20004
	v_writelane_b32 v253, s1, 41
	s_add_i32 s1, 0, 0x2000c
	v_writelane_b32 v253, s1, 42
	s_add_i32 s1, 0, 0x20014
	v_writelane_b32 v253, s1, 43
	s_add_i32 s1, 0, 0x2001c
	v_writelane_b32 v253, s1, 44
	s_add_i32 s1, 0, 0x20024
	v_writelane_b32 v253, s1, 45
	s_add_i32 s1, 0, 0x2002c
	v_writelane_b32 v253, s1, 46
	s_add_i32 s1, 0, 0x20034
	v_writelane_b32 v253, s1, 47
	s_add_i32 s1, 0, 0x2003c
	v_writelane_b32 v253, s1, 48
	s_add_i32 s1, 0, 0x20044
	v_writelane_b32 v253, s1, 49
	s_add_i32 s1, 0, 0x2004c
	v_writelane_b32 v253, s1, 50
	s_add_i32 s1, 0, 0x20054
	s_and_b32 s0, s0, 0xc0000
	v_writelane_b32 v253, s1, 51
	s_add_i32 s1, 0, 0x2005c
	v_writelane_b32 v253, s1, 52
	s_lshl_b32 s0, s0, 1
	v_writelane_b32 v253, s0, 53
	s_add_i32 s69, 0, 0x14100
	v_mov_b32_e32 v1, 0x358637bd
	v_writelane_b32 v253, s1, 54
	s_mov_b32 s0, 0
	v_writelane_b32 v253, s0, 55
	s_mov_b32 s0, s8
	v_writelane_b32 v253, s0, 56
	s_mov_b64 s[4:5], 0
	s_mov_b32 s84, 0x3b808081
	v_writelane_b32 v253, s1, 57
	s_lshl_b64 s[0:1], s[8:9], 19
	v_writelane_b32 v253, s0, 58
	s_nop 1
	v_writelane_b32 v253, s1, 59
	s_mov_b64 s[0:1], -1
	v_writelane_b32 v253, s0, 60
	s_nop 1
	v_writelane_b32 v253, s1, 61
	v_writelane_b32 v253, s69, 62
	v_writelane_b32 v253, s92, 63
	s_nop 1
	v_writelane_b32 v254, s93, 0
	v_writelane_b32 v254, s94, 1
	s_nop 1
	v_writelane_b32 v254, s95, 2
	s_branch .LBB0_213

.LBB0_2131:
	s_add_i32 s40, s40, 1
	v_readlane_b32 s7, v252, 61
	s_mul_i32 s7, s40, s7
	v_readlane_b32 s8, v252, 62
	s_add_i32 s7, s7, s8
	s_cmp_lt_i32 s7, 64
	s_cselect_b64 s[10:11], -1, 0
	s_cmp_gt_i32 s7, 63
	s_cselect_b64 s[8:9], -1, 0
	s_and_b64 vcc, exec, s[8:9]
	s_cbranch_vccnz .LBB0_2133
	v_readlane_b32 s15, v252, 52
	s_lshr_b32 s100, s7, 5
	s_lshr_b32 s101, s15, 4
	s_add_i32 s100, s100, s101
	s_and_b32 s100, s100, 1
	s_lshl_b32 s100, s100, 1
	s_and_b32 s101, s7, 31
	s_and_b32 s14, s101, 15
	s_add_i32 s41, s14, s15
	s_lshr_b32 s101, s101, 4
	s_add_i32 s6, s100, s101
